# dilated attention: band-edge masks folded into the bias table as -1e30 entries (exp2 underflows to exactly 0); explicit mask code skipped
# baseline (speedup 1.0000x reference)
.LBB0_264:
	v_mul_hi_i32 v3, v2, s16
	v_lshrrev_b32_e32 v4, 31, v3
	v_ashrrev_i32_e32 v3, 5, v3
	v_add_u32_e32 v3, v3, v4
	v_mad_u64_u32 v[4:5], s[12:13], v3, s17, v[2:3]
	v_cmp_gt_i32_e32 vcc, s18, v4
	v_mov_b32_e32 v5, 0xf149f2ca
	s_and_saveexec_b64 s[12:13], vcc
	s_cbranch_execz .LBB0_263
	v_and_b32_e32 v5, -4, v3
	v_cmp_eq_u32_e32 vcc, 4, v5
	s_nop 1
	v_cndmask_b32_e64 v5, 4, 2, vcc
	v_cmp_lt_u32_e32 vcc, 3, v3
	s_nop 1
	v_cndmask_b32_e32 v5, 0, v5, vcc
	v_lshlrev_b32_e32 v4, v5, v4
	v_cmp_lt_i32_e32 vcc, 15, v4
	s_and_saveexec_b64 s[14:15], vcc
	s_cbranch_execz .LBB0_262
	v_cvt_f32_u32_e32 v4, v4
	v_mul_f32_e32 v4, 0x3d800000, v4
	v_cmp_gt_f32_e32 vcc, s19, v4
	s_nop 1
	v_cndmask_b32_e64 v5, 0, 32, vcc
	v_ldexp_f32 v4, v4, v5
	v_log_f32_e32 v4, v4
	v_cndmask_b32_e32 v5, 0, v6, vcc
	v_mul_f32_e32 v7, 0x3f317217, v4
	v_fma_f32 v7, v4, s23, -v7
	v_fmac_f32_e32 v7, 0x3377d1cf, v4
	v_fmac_f32_e32 v7, 0x3f317217, v4
	v_cmp_lt_f32_e64 vcc, |v4|, s24
	s_nop 1
	v_cndmask_b32_e32 v4, v4, v7, vcc
	v_sub_f32_e32 v4, v4, v5
	v_div_scale_f32 v5, s[30:31], s25, s25, v4
	v_rcp_f32_e32 v7, v5
	v_div_scale_f32 v10, vcc, v4, s25, v4
	v_fma_f32 v11, -v5, v7, 1.0
	v_fmac_f32_e32 v7, v11, v7
	v_mul_f32_e32 v11, v10, v7
	v_fma_f32 v12, -v5, v11, v10
	v_fmac_f32_e32 v11, v12, v7
	v_fma_f32 v5, -v5, v11, v10
	v_div_fmas_f32 v5, v5, v7, v11
	v_div_fixup_f32 v4, v5, s25, v4
	v_mul_f32_e32 v4, 0x41800000, v4
	v_cvt_i32_f32_e32 v4, v4
	v_min_i32_e32 v4, 15, v4
	v_add_u32_e32 v4, 16, v4
	s_branch .LBB0_262

.LBB0_1520:
	s_or_b64 exec, exec, s[34:35]
	s_ashr_i32 s50, s41, 6
	s_lshl_b32 s51, s82, 8
	s_lshl_b32 s46, s50, 5
	s_lshl_b32 s36, s83, 11
	s_add_i32 s46, s46, s51
	s_and_b64 s[34:35], s[4:5], exec
	s_movk_i32 s34, 0x80
	s_cselect_b32 s37, 0x200, s34
	s_and_b64 s[34:35], s[10:11], exec
	v_and_b32_e32 v138, 31, v4
	s_cselect_b32 s47, 0x800, s37
	s_and_b64 s[4:5], s[4:5], exec
	v_or_b32_e32 v136, s46, v138
	s_cselect_b32 s34, 2, 4
	s_and_b64 s[4:5], s[10:11], exec
	v_cmp_gt_i32_e32 vcc, s47, v136
	s_cselect_b32 s45, 0, s34
	s_lshl_b32 s4, s40, 23
	v_cndmask_b32_e32 v2, 0, v136, vcc
	s_add_u32 s4, s16, s4
	v_lshlrev_b32_e32 v2, s45, v2
	s_addc_u32 s5, s17, 0
	s_or_b32 s35, s36, s7
	v_add_u32_e32 v8, s35, v2
	v_ashrrev_i32_e32 v9, 31, v8
	v_lshlrev_b64 v[8:9], 9, v[8:9]
	v_bfe_u32 v6, v4, 5, 1
	v_lshl_add_u64 v[8:9], s[4:5], 0, v[8:9]
	s_lshl_b32 s48, s6, 7
	v_lshl_add_u64 v[8:9], v[8:9], 0, s[48:49]
	v_lshlrev_b32_e32 v2, 4, v6
	v_lshl_add_u64 v[8:9], v[8:9], 0, v[2:3]
	s_mov_b64 s[10:11], 0x4000000
	v_lshl_add_u64 v[132:133], v[8:9], 0, s[10:11]
	v_add_co_u32_e32 v8, vcc, 0x4000000, v8
	s_movk_i32 s10, 0x100
	s_nop 0
	v_addc_co_u32_e32 v9, vcc, 0, v9, vcc
	global_load_dwordx4 v[116:119], v[132:133], off offset:32
	global_load_dwordx4 v[120:123], v[132:133], off offset:64
	global_load_dwordx4 v[124:127], v[8:9], off
	global_load_dwordx4 v[128:131], v[132:133], off offset:96
	s_lshl_b32 s34, s40, 2
	v_cmp_gt_i32_e32 vcc, s10, v4
	s_and_saveexec_b64 s[10:11], vcc
	s_cbranch_execz .LBB0_1524
	v_cmp_lt_i32_e32 vcc, 63, v4
	v_mov_b32_e32 v2, 0xf149f2ca
	s_and_saveexec_b64 s[38:39], vcc
	s_cbranch_execz .LBB0_1523
	s_or_b32 s37, s34, s6
	s_mul_i32 s48, s37, 0xc0
	s_lshl_b64 s[40:41], s[48:49], 2
	s_add_u32 s40, s0, s40
	s_addc_u32 s41, s1, s41
	v_mov_b32_e32 v5, v3
	v_lshl_add_u64 v[8:9], v[4:5], 2, s[40:41]
	v_add_co_u32_e32 v8, vcc, 0x129000, v8
	s_nop 1
	v_addc_co_u32_e32 v9, vcc, 0, v9, vcc
	global_load_dword v2, v[8:9], off offset:768
